# baseline (speedup 1.0000x reference)
.LBB2_23:
	v_readfirstlane_b32 s80, v177
	s_cmp_lt_u32 s80, 4
	s_cbranch_scc1 .Lat_nostag
	s_sleep 4
